# NA phase V staging: 12 global loads in flight per unit instead of serialized load/wait/ds_write
# speedup vs baseline: 1.0126x; 1.0102x over previous
.LBB0_395:
	v_med3_u32 v2, s68, 4, 28
	s_and_b32 s71, s50, 3
	v_readfirstlane_b32 s72, v2
	s_add_i32 s72, s72, -4
	v_cmp_gt_i32_e32 vcc, s66, v74
	s_barrier
	s_and_saveexec_b64 s[60:61], vcc
	s_cbranch_execz .LBB0_406
	s_lshl_b32 s73, s69, 8
	s_lshl_b32 s50, s71, 7
	s_add_i32 s67, s73, 0x4000
	s_addk_i32 s73, 0x3e00
	s_lshl_b32 s74, s69, 11
	v_lshl_add_u64 v[2:3], v[76:77], 0, s[50:51]
	v_lshrrev_b32_e32 v5, 3, v74
	v_mad_u64_u32 v[10:11], s[64:65], v5, s84, v[70:71]
	v_add_u32_e32 v11, 0x12000, v10
	s_and_b64 vcc, exec, s[48:49]
	s_cbranch_vccnz .Lnastg0_ctx
	s_lshl_b32 s62, s72, 6
	s_add_i32 s62, s62, s74
	v_add_u32_e32 v6, s62, v5
	v_mad_i64_i32 v[6:7], s[64:65], v6, s86, v[2:3]
	global_load_dwordx4 v[108:111], v[6:7], off offset:1536
	s_addk_i32 s62, 0x40
	v_add_u32_e32 v6, s62, v5
	v_mad_i64_i32 v[6:7], s[64:65], v6, s86, v[2:3]
	global_load_dwordx4 v[112:115], v[6:7], off offset:1536
	s_addk_i32 s62, 0x40
	v_add_u32_e32 v6, s62, v5
	v_mad_i64_i32 v[6:7], s[64:65], v6, s86, v[2:3]
	global_load_dwordx4 v[116:119], v[6:7], off offset:1536
	s_addk_i32 s62, 0x40
	v_add_u32_e32 v6, s62, v5
	v_mad_i64_i32 v[6:7], s[64:65], v6, s86, v[2:3]
	global_load_dwordx4 v[120:123], v[6:7], off offset:1536
	s_addk_i32 s62, 0x40
	v_add_u32_e32 v6, s62, v5
	v_mad_i64_i32 v[6:7], s[64:65], v6, s86, v[2:3]
	global_load_dwordx4 v[124:127], v[6:7], off offset:1536
	s_addk_i32 s62, 0x40
	v_add_u32_e32 v6, s62, v5
	v_mad_i64_i32 v[6:7], s[64:65], v6, s86, v[2:3]
	global_load_dwordx4 v[128:131], v[6:7], off offset:1536
	s_addk_i32 s62, 0x40
	v_add_u32_e32 v6, s62, v5
	v_mad_i64_i32 v[6:7], s[64:65], v6, s86, v[2:3]
	global_load_dwordx4 v[132:135], v[6:7], off offset:1536
	s_addk_i32 s62, 0x40
	v_add_u32_e32 v6, s62, v5
	v_mad_i64_i32 v[6:7], s[64:65], v6, s86, v[2:3]
	global_load_dwordx4 v[136:139], v[6:7], off offset:1536
	s_addk_i32 s62, 0x40
	s_add_i32 s62, s73, 0x200
	v_add_u32_e32 v6, s62, v5
	v_mad_i64_i32 v[6:7], s[64:65], v6, s86, v[2:3]
	global_load_dwordx4 v[140:143], v[6:7], off offset:1536
	s_addk_i32 s62, 0x40
	v_add_u32_e32 v6, s62, v5
	v_mad_i64_i32 v[6:7], s[64:65], v6, s86, v[2:3]
	global_load_dwordx4 v[144:147], v[6:7], off offset:1536
	s_addk_i32 s62, 0x40
	v_add_u32_e32 v6, s62, v5
	v_mad_i64_i32 v[6:7], s[64:65], v6, s86, v[2:3]
	global_load_dwordx4 v[148:151], v[6:7], off offset:1536
	s_addk_i32 s62, 0x40
	v_add_u32_e32 v6, s62, v5
	v_mad_i64_i32 v[6:7], s[64:65], v6, s86, v[2:3]
	global_load_dwordx4 v[152:155], v[6:7], off offset:1536
	s_waitcnt vmcnt(11)
	ds_write_b128 v10, v[108:111]
	s_waitcnt vmcnt(10)
	ds_write_b128 v10, v[112:115] offset:9216
	s_waitcnt vmcnt(9)
	ds_write_b128 v10, v[116:119] offset:18432
	s_waitcnt vmcnt(8)
	ds_write_b128 v10, v[120:123] offset:27648
	s_waitcnt vmcnt(7)
	ds_write_b128 v10, v[124:127] offset:36864
	s_waitcnt vmcnt(6)
	ds_write_b128 v10, v[128:131] offset:46080
	s_waitcnt vmcnt(5)
	ds_write_b128 v10, v[132:135] offset:55296
	s_waitcnt vmcnt(4)
	ds_write_b128 v10, v[136:139] offset:64512
	s_waitcnt vmcnt(3)
	ds_write_b128 v11, v[140:143]
	s_waitcnt vmcnt(2)
	ds_write_b128 v11, v[144:147] offset:9216
	s_waitcnt vmcnt(1)
	ds_write_b128 v11, v[148:151] offset:18432
	s_waitcnt vmcnt(0)
	ds_write_b128 v11, v[152:155] offset:27648
	s_branch .LBB0_406
.Lnastg0_ctx:
	s_mov_b32 s62, s67
	v_add_u32_e32 v6, s62, v5
	v_mad_i64_i32 v[6:7], s[64:65], v6, s86, v[2:3]
	global_load_dwordx4 v[108:111], v[6:7], off offset:1536
	s_addk_i32 s62, 0x40
	v_add_u32_e32 v6, s62, v5
	v_mad_i64_i32 v[6:7], s[64:65], v6, s86, v[2:3]
	global_load_dwordx4 v[112:115], v[6:7], off offset:1536
	s_addk_i32 s62, 0x40
	v_add_u32_e32 v6, s62, v5
	v_mad_i64_i32 v[6:7], s[64:65], v6, s86, v[2:3]
	global_load_dwordx4 v[116:119], v[6:7], off offset:1536
	s_addk_i32 s62, 0x40
	v_add_u32_e32 v6, s62, v5
	v_mad_i64_i32 v[6:7], s[64:65], v6, s86, v[2:3]
	global_load_dwordx4 v[120:123], v[6:7], off offset:1536
	s_waitcnt vmcnt(3)
	ds_write_b128 v10, v[108:111]
	s_waitcnt vmcnt(2)
	ds_write_b128 v10, v[112:115] offset:9216
	s_waitcnt vmcnt(1)
	ds_write_b128 v10, v[116:119] offset:18432
	s_waitcnt vmcnt(0)
	ds_write_b128 v10, v[120:123] offset:27648

.LBB0_4806:
	s_bfe_u32 s71, s69, 0x50002
	v_med3_u32 v2, s71, 4, 28
	s_ashr_i32 s72, s69, 7
	v_readfirstlane_b32 s74, v2
	s_and_b32 s70, s69, 3
	s_add_i32 s74, s74, -4
	s_lshl_b32 s73, s72, 11
	s_barrier
	s_and_saveexec_b64 s[30:31], s[4:5]
	s_cbranch_execz .LBB0_4813
	s_lshl_b32 s52, s72, 8
	s_lshl_b32 s40, s70, 7
	s_addk_i32 s52, 0x3e00
	v_lshl_add_u64 v[2:3], v[90:91], 0, s[40:41]
	v_lshrrev_b32_e32 v5, 3, v74
	v_mad_u64_u32 v[10:11], s[50:51], v5, s60, v[68:69]
	v_add_u32_e32 v11, 0x12000, v10
	s_lshl_b32 s34, s74, 6
	s_add_i32 s34, s34, s73
	v_add_u32_e32 v6, s34, v5
	v_mad_i64_i32 v[6:7], s[50:51], v6, s62, v[2:3]
	global_load_dwordx4 v[114:117], v[6:7], off offset:1536
	s_addk_i32 s34, 0x40
	v_add_u32_e32 v6, s34, v5
	v_mad_i64_i32 v[6:7], s[50:51], v6, s62, v[2:3]
	global_load_dwordx4 v[118:121], v[6:7], off offset:1536
	s_addk_i32 s34, 0x40
	v_add_u32_e32 v6, s34, v5
	v_mad_i64_i32 v[6:7], s[50:51], v6, s62, v[2:3]
	global_load_dwordx4 v[122:125], v[6:7], off offset:1536
	s_addk_i32 s34, 0x40
	v_add_u32_e32 v6, s34, v5
	v_mad_i64_i32 v[6:7], s[50:51], v6, s62, v[2:3]
	global_load_dwordx4 v[126:129], v[6:7], off offset:1536
	s_addk_i32 s34, 0x40
	v_add_u32_e32 v6, s34, v5
	v_mad_i64_i32 v[6:7], s[50:51], v6, s62, v[2:3]
	global_load_dwordx4 v[130:133], v[6:7], off offset:1536
	s_addk_i32 s34, 0x40
	v_add_u32_e32 v6, s34, v5
	v_mad_i64_i32 v[6:7], s[50:51], v6, s62, v[2:3]
	global_load_dwordx4 v[134:137], v[6:7], off offset:1536
	s_addk_i32 s34, 0x40
	v_add_u32_e32 v6, s34, v5
	v_mad_i64_i32 v[6:7], s[50:51], v6, s62, v[2:3]
	global_load_dwordx4 v[138:141], v[6:7], off offset:1536
	s_addk_i32 s34, 0x40
	v_add_u32_e32 v6, s34, v5
	v_mad_i64_i32 v[6:7], s[50:51], v6, s62, v[2:3]
	global_load_dwordx4 v[142:145], v[6:7], off offset:1536
	s_addk_i32 s34, 0x40
	s_add_i32 s34, s52, 0x200
	v_add_u32_e32 v6, s34, v5
	v_mad_i64_i32 v[6:7], s[50:51], v6, s62, v[2:3]
	global_load_dwordx4 v[146:149], v[6:7], off offset:1536
	s_addk_i32 s34, 0x40
	v_add_u32_e32 v6, s34, v5
	v_mad_i64_i32 v[6:7], s[50:51], v6, s62, v[2:3]
	global_load_dwordx4 v[150:153], v[6:7], off offset:1536
	s_addk_i32 s34, 0x40
	v_add_u32_e32 v6, s34, v5
	v_mad_i64_i32 v[6:7], s[50:51], v6, s62, v[2:3]
	global_load_dwordx4 v[154:157], v[6:7], off offset:1536
	s_addk_i32 s34, 0x40
	v_add_u32_e32 v6, s34, v5
	v_mad_i64_i32 v[6:7], s[50:51], v6, s62, v[2:3]
	global_load_dwordx4 v[158:161], v[6:7], off offset:1536
	s_waitcnt vmcnt(11)
	ds_write_b128 v10, v[114:117]
	s_waitcnt vmcnt(10)
	ds_write_b128 v10, v[118:121] offset:9216
	s_waitcnt vmcnt(9)
	ds_write_b128 v10, v[122:125] offset:18432
	s_waitcnt vmcnt(8)
	ds_write_b128 v10, v[126:129] offset:27648
	s_waitcnt vmcnt(7)
	ds_write_b128 v10, v[130:133] offset:36864
	s_waitcnt vmcnt(6)
	ds_write_b128 v10, v[134:137] offset:46080
	s_waitcnt vmcnt(5)
	ds_write_b128 v10, v[138:141] offset:55296
	s_waitcnt vmcnt(4)
	ds_write_b128 v10, v[142:145] offset:64512
	s_waitcnt vmcnt(3)
	ds_write_b128 v11, v[146:149]
	s_waitcnt vmcnt(2)
	ds_write_b128 v11, v[150:153] offset:9216
	s_waitcnt vmcnt(1)
	ds_write_b128 v11, v[154:157] offset:18432
	s_waitcnt vmcnt(0)
	ds_write_b128 v11, v[158:161] offset:27648
